# P0 adaLN: batch 32 silu loads, software-pipeline GEMV k-loop (2 load sets in flight)
# speedup vs baseline: 1.0052x; 1.0052x over previous
; #define LAS __attribute__((address_space(3)))
; __device__ __forceinline__ void p0_prologue(Frame& F) {
;     float* mod = (float*)(F.ws + WS_MOD);
;     const float* Fc = inptr<const float>(F, I_C); const float* Fw_ada = inptr<const float>(F, I_WADA); const float* Fb_ada = inptr<const float>(F, I_BADA);
;     {
;         LAS float* cact = (LAS float*)(F.lds);
;         LAS float* part = (LAS float*)(F.lds + 65536);
;         for (int i = F.tid; i < NB * D; i += NWAVES * 64) { const float v = Fc[i]; cact[i] = v / (1.f + __expf(-v)); }
;         __syncthreads();
.LBB0_16:
	global_load_dword v128, v[0:1], off
	v_lshl_add_u64 v[0:1], v[0:1], 0, s[8:9]
	global_load_dword v129, v[0:1], off
	v_lshl_add_u64 v[0:1], v[0:1], 0, s[8:9]
	global_load_dword v130, v[0:1], off
	v_lshl_add_u64 v[0:1], v[0:1], 0, s[8:9]
	global_load_dword v131, v[0:1], off
	v_lshl_add_u64 v[0:1], v[0:1], 0, s[8:9]
	global_load_dword v132, v[0:1], off
	v_lshl_add_u64 v[0:1], v[0:1], 0, s[8:9]
	global_load_dword v133, v[0:1], off
	v_lshl_add_u64 v[0:1], v[0:1], 0, s[8:9]
	global_load_dword v134, v[0:1], off
	v_lshl_add_u64 v[0:1], v[0:1], 0, s[8:9]
	global_load_dword v135, v[0:1], off
	v_lshl_add_u64 v[0:1], v[0:1], 0, s[8:9]
	global_load_dword v136, v[0:1], off
	v_lshl_add_u64 v[0:1], v[0:1], 0, s[8:9]
	global_load_dword v137, v[0:1], off
	v_lshl_add_u64 v[0:1], v[0:1], 0, s[8:9]
	global_load_dword v138, v[0:1], off
	v_lshl_add_u64 v[0:1], v[0:1], 0, s[8:9]
	global_load_dword v139, v[0:1], off
	v_lshl_add_u64 v[0:1], v[0:1], 0, s[8:9]
	global_load_dword v140, v[0:1], off
	v_lshl_add_u64 v[0:1], v[0:1], 0, s[8:9]
	global_load_dword v141, v[0:1], off
	v_lshl_add_u64 v[0:1], v[0:1], 0, s[8:9]
	global_load_dword v142, v[0:1], off
	v_lshl_add_u64 v[0:1], v[0:1], 0, s[8:9]
	global_load_dword v143, v[0:1], off
	v_lshl_add_u64 v[0:1], v[0:1], 0, s[8:9]
	global_load_dword v144, v[0:1], off
	v_lshl_add_u64 v[0:1], v[0:1], 0, s[8:9]
	global_load_dword v145, v[0:1], off
	v_lshl_add_u64 v[0:1], v[0:1], 0, s[8:9]
	global_load_dword v146, v[0:1], off
	v_lshl_add_u64 v[0:1], v[0:1], 0, s[8:9]
	global_load_dword v147, v[0:1], off
	v_lshl_add_u64 v[0:1], v[0:1], 0, s[8:9]
	global_load_dword v148, v[0:1], off
	v_lshl_add_u64 v[0:1], v[0:1], 0, s[8:9]
	global_load_dword v149, v[0:1], off
	v_lshl_add_u64 v[0:1], v[0:1], 0, s[8:9]
	global_load_dword v150, v[0:1], off
	v_lshl_add_u64 v[0:1], v[0:1], 0, s[8:9]
	global_load_dword v151, v[0:1], off
	v_lshl_add_u64 v[0:1], v[0:1], 0, s[8:9]
	global_load_dword v152, v[0:1], off
	v_lshl_add_u64 v[0:1], v[0:1], 0, s[8:9]
	global_load_dword v153, v[0:1], off
	v_lshl_add_u64 v[0:1], v[0:1], 0, s[8:9]
	global_load_dword v154, v[0:1], off
	v_lshl_add_u64 v[0:1], v[0:1], 0, s[8:9]
	global_load_dword v155, v[0:1], off
	v_lshl_add_u64 v[0:1], v[0:1], 0, s[8:9]
	global_load_dword v156, v[0:1], off
	v_lshl_add_u64 v[0:1], v[0:1], 0, s[8:9]
	global_load_dword v157, v[0:1], off
	v_lshl_add_u64 v[0:1], v[0:1], 0, s[8:9]
	global_load_dword v158, v[0:1], off
	v_lshl_add_u64 v[0:1], v[0:1], 0, s[8:9]
	global_load_dword v159, v[0:1], off
	s_waitcnt vmcnt(31)
	v_mul_f32_e32 v5, 0xbfb8aa3b, v128
	v_exp_f32_e32 v5, v5
	s_nop 0
	v_add_f32_e32 v5, 1.0, v5
	v_div_scale_f32 v6, s[12:13], v5, v5, v128
	v_rcp_f32_e32 v7, v6
	v_div_scale_f32 v8, vcc, v128, v5, v128
	v_fma_f32 v9, -v6, v7, 1.0
	v_fmac_f32_e32 v7, v9, v7
	v_mul_f32_e32 v9, v8, v7
	v_fma_f32 v10, -v6, v9, v8
	v_fmac_f32_e32 v9, v10, v7
	v_fma_f32 v6, -v6, v9, v8
	v_div_fmas_f32 v6, v6, v7, v9
	v_div_fixup_f32 v4, v6, v5, v128
	ds_write_b32 v3, v4 offset:0
	s_waitcnt vmcnt(30)
	v_mul_f32_e32 v5, 0xbfb8aa3b, v129
	v_exp_f32_e32 v5, v5
	s_nop 0
	v_add_f32_e32 v5, 1.0, v5
	v_div_scale_f32 v6, s[12:13], v5, v5, v129
	v_rcp_f32_e32 v7, v6
	v_div_scale_f32 v8, vcc, v129, v5, v129
	v_fma_f32 v9, -v6, v7, 1.0
	v_fmac_f32_e32 v7, v9, v7
	v_mul_f32_e32 v9, v8, v7
	v_fma_f32 v10, -v6, v9, v8
	v_fmac_f32_e32 v9, v10, v7
	v_fma_f32 v6, -v6, v9, v8
	v_div_fmas_f32 v6, v6, v7, v9
	v_div_fixup_f32 v4, v6, v5, v129
	ds_write_b32 v3, v4 offset:2048
	s_waitcnt vmcnt(29)
	v_mul_f32_e32 v5, 0xbfb8aa3b, v130
	v_exp_f32_e32 v5, v5
	s_nop 0
	v_add_f32_e32 v5, 1.0, v5
	v_div_scale_f32 v6, s[12:13], v5, v5, v130
	v_rcp_f32_e32 v7, v6
	v_div_scale_f32 v8, vcc, v130, v5, v130
	v_fma_f32 v9, -v6, v7, 1.0
	v_fmac_f32_e32 v7, v9, v7
	v_mul_f32_e32 v9, v8, v7
	v_fma_f32 v10, -v6, v9, v8
	v_fmac_f32_e32 v9, v10, v7
	v_fma_f32 v6, -v6, v9, v8
	v_div_fmas_f32 v6, v6, v7, v9
	v_div_fixup_f32 v4, v6, v5, v130
	ds_write_b32 v3, v4 offset:4096
	s_waitcnt vmcnt(28)
	v_mul_f32_e32 v5, 0xbfb8aa3b, v131
	v_exp_f32_e32 v5, v5
	s_nop 0
	v_add_f32_e32 v5, 1.0, v5
	v_div_scale_f32 v6, s[12:13], v5, v5, v131
	v_rcp_f32_e32 v7, v6
	v_div_scale_f32 v8, vcc, v131, v5, v131
	v_fma_f32 v9, -v6, v7, 1.0
	v_fmac_f32_e32 v7, v9, v7
	v_mul_f32_e32 v9, v8, v7
	v_fma_f32 v10, -v6, v9, v8
	v_fmac_f32_e32 v9, v10, v7
	v_fma_f32 v6, -v6, v9, v8
	v_div_fmas_f32 v6, v6, v7, v9
	v_div_fixup_f32 v4, v6, v5, v131
	ds_write_b32 v3, v4 offset:6144
	s_waitcnt vmcnt(27)
	v_mul_f32_e32 v5, 0xbfb8aa3b, v132
	v_exp_f32_e32 v5, v5
	s_nop 0
	v_add_f32_e32 v5, 1.0, v5
	v_div_scale_f32 v6, s[12:13], v5, v5, v132
	v_rcp_f32_e32 v7, v6
	v_div_scale_f32 v8, vcc, v132, v5, v132
	v_fma_f32 v9, -v6, v7, 1.0
	v_fmac_f32_e32 v7, v9, v7
	v_mul_f32_e32 v9, v8, v7
	v_fma_f32 v10, -v6, v9, v8
	v_fmac_f32_e32 v9, v10, v7
	v_fma_f32 v6, -v6, v9, v8
	v_div_fmas_f32 v6, v6, v7, v9
	v_div_fixup_f32 v4, v6, v5, v132
	ds_write_b32 v3, v4 offset:8192
	s_waitcnt vmcnt(26)
	v_mul_f32_e32 v5, 0xbfb8aa3b, v133
	v_exp_f32_e32 v5, v5
	s_nop 0
	v_add_f32_e32 v5, 1.0, v5
	v_div_scale_f32 v6, s[12:13], v5, v5, v133
	v_rcp_f32_e32 v7, v6
	v_div_scale_f32 v8, vcc, v133, v5, v133
	v_fma_f32 v9, -v6, v7, 1.0
	v_fmac_f32_e32 v7, v9, v7
	v_mul_f32_e32 v9, v8, v7
	v_fma_f32 v10, -v6, v9, v8
	v_fmac_f32_e32 v9, v10, v7
	v_fma_f32 v6, -v6, v9, v8
	v_div_fmas_f32 v6, v6, v7, v9
	v_div_fixup_f32 v4, v6, v5, v133
	ds_write_b32 v3, v4 offset:10240
	s_waitcnt vmcnt(25)
; __device__ __forceinline__ void p0_prologue(Frame& F) {
;     ...
;         for (int i = F.tid; i < NB * D; i += NWAVES * 64) { const float v = Fc[i]; cact[i] = v / (1.f + __expf(-v)); }
	v_mul_f32_e32 v5, 0xbfb8aa3b, v134
	v_exp_f32_e32 v5, v5
	s_nop 0
	v_add_f32_e32 v5, 1.0, v5
	v_div_scale_f32 v6, s[12:13], v5, v5, v134
	v_rcp_f32_e32 v7, v6
	v_div_scale_f32 v8, vcc, v134, v5, v134
	v_fma_f32 v9, -v6, v7, 1.0
	v_fmac_f32_e32 v7, v9, v7
	v_mul_f32_e32 v9, v8, v7
	v_fma_f32 v10, -v6, v9, v8
	v_fmac_f32_e32 v9, v10, v7
	v_fma_f32 v6, -v6, v9, v8
	v_div_fmas_f32 v6, v6, v7, v9
	v_div_fixup_f32 v4, v6, v5, v134
	ds_write_b32 v3, v4 offset:12288
	s_waitcnt vmcnt(24)
	v_mul_f32_e32 v5, 0xbfb8aa3b, v135
	v_exp_f32_e32 v5, v5
	s_nop 0
	v_add_f32_e32 v5, 1.0, v5
	v_div_scale_f32 v6, s[12:13], v5, v5, v135
	v_rcp_f32_e32 v7, v6
	v_div_scale_f32 v8, vcc, v135, v5, v135
	v_fma_f32 v9, -v6, v7, 1.0
	v_fmac_f32_e32 v7, v9, v7
	v_mul_f32_e32 v9, v8, v7
	v_fma_f32 v10, -v6, v9, v8
	v_fmac_f32_e32 v9, v10, v7
	v_fma_f32 v6, -v6, v9, v8
	v_div_fmas_f32 v6, v6, v7, v9
	v_div_fixup_f32 v4, v6, v5, v135
	ds_write_b32 v3, v4 offset:14336
	s_waitcnt vmcnt(23)
	v_mul_f32_e32 v5, 0xbfb8aa3b, v136
	v_exp_f32_e32 v5, v5
	s_nop 0
	v_add_f32_e32 v5, 1.0, v5
	v_div_scale_f32 v6, s[12:13], v5, v5, v136
	v_rcp_f32_e32 v7, v6
	v_div_scale_f32 v8, vcc, v136, v5, v136
	v_fma_f32 v9, -v6, v7, 1.0
	v_fmac_f32_e32 v7, v9, v7
	v_mul_f32_e32 v9, v8, v7
	v_fma_f32 v10, -v6, v9, v8
	v_fmac_f32_e32 v9, v10, v7
	v_fma_f32 v6, -v6, v9, v8
	v_div_fmas_f32 v6, v6, v7, v9
	v_div_fixup_f32 v4, v6, v5, v136
	ds_write_b32 v3, v4 offset:16384
	s_waitcnt vmcnt(22)
	v_mul_f32_e32 v5, 0xbfb8aa3b, v137
	v_exp_f32_e32 v5, v5
	s_nop 0
	v_add_f32_e32 v5, 1.0, v5
	v_div_scale_f32 v6, s[12:13], v5, v5, v137
	v_rcp_f32_e32 v7, v6
	v_div_scale_f32 v8, vcc, v137, v5, v137
	v_fma_f32 v9, -v6, v7, 1.0
	v_fmac_f32_e32 v7, v9, v7
	v_mul_f32_e32 v9, v8, v7
	v_fma_f32 v10, -v6, v9, v8
	v_fmac_f32_e32 v9, v10, v7
	v_fma_f32 v6, -v6, v9, v8
	v_div_fmas_f32 v6, v6, v7, v9
	v_div_fixup_f32 v4, v6, v5, v137
	ds_write_b32 v3, v4 offset:18432
	s_waitcnt vmcnt(21)
	v_mul_f32_e32 v5, 0xbfb8aa3b, v138
	v_exp_f32_e32 v5, v5
	s_nop 0
	v_add_f32_e32 v5, 1.0, v5
	v_div_scale_f32 v6, s[12:13], v5, v5, v138
	v_rcp_f32_e32 v7, v6
	v_div_scale_f32 v8, vcc, v138, v5, v138
	v_fma_f32 v9, -v6, v7, 1.0
	v_fmac_f32_e32 v7, v9, v7
	v_mul_f32_e32 v9, v8, v7
	v_fma_f32 v10, -v6, v9, v8
	v_fmac_f32_e32 v9, v10, v7
	v_fma_f32 v6, -v6, v9, v8
	v_div_fmas_f32 v6, v6, v7, v9
	v_div_fixup_f32 v4, v6, v5, v138
	ds_write_b32 v3, v4 offset:20480
	s_waitcnt vmcnt(20)
	v_mul_f32_e32 v5, 0xbfb8aa3b, v139
	v_exp_f32_e32 v5, v5
	s_nop 0
	v_add_f32_e32 v5, 1.0, v5
	v_div_scale_f32 v6, s[12:13], v5, v5, v139
	v_rcp_f32_e32 v7, v6
	v_div_scale_f32 v8, vcc, v139, v5, v139
	v_fma_f32 v9, -v6, v7, 1.0
	v_fmac_f32_e32 v7, v9, v7
	v_mul_f32_e32 v9, v8, v7
	v_fma_f32 v10, -v6, v9, v8
	v_fmac_f32_e32 v9, v10, v7
	v_fma_f32 v6, -v6, v9, v8
	v_div_fmas_f32 v6, v6, v7, v9
	v_div_fixup_f32 v4, v6, v5, v139
	ds_write_b32 v3, v4 offset:22528
	s_waitcnt vmcnt(19)
	v_mul_f32_e32 v5, 0xbfb8aa3b, v140
	v_exp_f32_e32 v5, v5
	s_nop 0
	v_add_f32_e32 v5, 1.0, v5
	v_div_scale_f32 v6, s[12:13], v5, v5, v140
	v_rcp_f32_e32 v7, v6
	v_div_scale_f32 v8, vcc, v140, v5, v140
	v_fma_f32 v9, -v6, v7, 1.0
	v_fmac_f32_e32 v7, v9, v7
	v_mul_f32_e32 v9, v8, v7
	v_fma_f32 v10, -v6, v9, v8
	v_fmac_f32_e32 v9, v10, v7
	v_fma_f32 v6, -v6, v9, v8
	v_div_fmas_f32 v6, v6, v7, v9
	v_div_fixup_f32 v4, v6, v5, v140
	ds_write_b32 v3, v4 offset:24576
	s_waitcnt vmcnt(18)
	v_mul_f32_e32 v5, 0xbfb8aa3b, v141
	v_exp_f32_e32 v5, v5
	s_nop 0
	v_add_f32_e32 v5, 1.0, v5
	v_div_scale_f32 v6, s[12:13], v5, v5, v141
	v_rcp_f32_e32 v7, v6
	v_div_scale_f32 v8, vcc, v141, v5, v141
	v_fma_f32 v9, -v6, v7, 1.0
	v_fmac_f32_e32 v7, v9, v7
	v_mul_f32_e32 v9, v8, v7
	v_fma_f32 v10, -v6, v9, v8
	v_fmac_f32_e32 v9, v10, v7
	v_fma_f32 v6, -v6, v9, v8
	v_div_fmas_f32 v6, v6, v7, v9
	v_div_fixup_f32 v4, v6, v5, v141
	ds_write_b32 v3, v4 offset:26624
	s_waitcnt vmcnt(17)
	v_mul_f32_e32 v5, 0xbfb8aa3b, v142
	v_exp_f32_e32 v5, v5
	s_nop 0
	v_add_f32_e32 v5, 1.0, v5
	v_div_scale_f32 v6, s[12:13], v5, v5, v142
	v_rcp_f32_e32 v7, v6
	v_div_scale_f32 v8, vcc, v142, v5, v142
	v_fma_f32 v9, -v6, v7, 1.0
	v_fmac_f32_e32 v7, v9, v7
	v_mul_f32_e32 v9, v8, v7
	v_fma_f32 v10, -v6, v9, v8
	v_fmac_f32_e32 v9, v10, v7
	v_fma_f32 v6, -v6, v9, v8
	v_div_fmas_f32 v6, v6, v7, v9
	v_div_fixup_f32 v4, v6, v5, v142
	ds_write_b32 v3, v4 offset:28672
	s_waitcnt vmcnt(16)
	v_mul_f32_e32 v5, 0xbfb8aa3b, v143
	v_exp_f32_e32 v5, v5
	s_nop 0
	v_add_f32_e32 v5, 1.0, v5
	v_div_scale_f32 v6, s[12:13], v5, v5, v143
	v_rcp_f32_e32 v7, v6
	v_div_scale_f32 v8, vcc, v143, v5, v143
	v_fma_f32 v9, -v6, v7, 1.0
	v_fmac_f32_e32 v7, v9, v7
	v_mul_f32_e32 v9, v8, v7
	v_fma_f32 v10, -v6, v9, v8
	v_fmac_f32_e32 v9, v10, v7
	v_fma_f32 v6, -v6, v9, v8
	v_div_fmas_f32 v6, v6, v7, v9
	v_div_fixup_f32 v4, v6, v5, v143
	ds_write_b32 v3, v4 offset:30720
	s_waitcnt vmcnt(15)
	v_mul_f32_e32 v5, 0xbfb8aa3b, v144
	v_exp_f32_e32 v5, v5
	s_nop 0
	v_add_f32_e32 v5, 1.0, v5
	v_div_scale_f32 v6, s[12:13], v5, v5, v144
	v_rcp_f32_e32 v7, v6
	v_div_scale_f32 v8, vcc, v144, v5, v144
	v_fma_f32 v9, -v6, v7, 1.0
	v_fmac_f32_e32 v7, v9, v7
	v_mul_f32_e32 v9, v8, v7
	v_fma_f32 v10, -v6, v9, v8
	v_fmac_f32_e32 v9, v10, v7
	v_fma_f32 v6, -v6, v9, v8
	v_div_fmas_f32 v6, v6, v7, v9
	v_div_fixup_f32 v4, v6, v5, v144
	ds_write_b32 v3, v4 offset:32768
	s_waitcnt vmcnt(14)
	v_mul_f32_e32 v5, 0xbfb8aa3b, v145
	v_exp_f32_e32 v5, v5
	s_nop 0
	v_add_f32_e32 v5, 1.0, v5
	v_div_scale_f32 v6, s[12:13], v5, v5, v145
	v_rcp_f32_e32 v7, v6
	v_div_scale_f32 v8, vcc, v145, v5, v145
	v_fma_f32 v9, -v6, v7, 1.0
	v_fmac_f32_e32 v7, v9, v7
	v_mul_f32_e32 v9, v8, v7
	v_fma_f32 v10, -v6, v9, v8
	v_fmac_f32_e32 v9, v10, v7
	v_fma_f32 v6, -v6, v9, v8
	v_div_fmas_f32 v6, v6, v7, v9
	v_div_fixup_f32 v4, v6, v5, v145
	ds_write_b32 v3, v4 offset:34816
	s_waitcnt vmcnt(13)
; __device__ __forceinline__ void p0_prologue(Frame& F) {
;     ...
;         for (int i = F.tid; i < NB * D; i += NWAVES * 64) { const float v = Fc[i]; cact[i] = v / (1.f + __expf(-v)); }
	v_mul_f32_e32 v5, 0xbfb8aa3b, v146
	v_exp_f32_e32 v5, v5
	s_nop 0
	v_add_f32_e32 v5, 1.0, v5
	v_div_scale_f32 v6, s[12:13], v5, v5, v146
	v_rcp_f32_e32 v7, v6
	v_div_scale_f32 v8, vcc, v146, v5, v146
	v_fma_f32 v9, -v6, v7, 1.0
	v_fmac_f32_e32 v7, v9, v7
	v_mul_f32_e32 v9, v8, v7
	v_fma_f32 v10, -v6, v9, v8
	v_fmac_f32_e32 v9, v10, v7
	v_fma_f32 v6, -v6, v9, v8
	v_div_fmas_f32 v6, v6, v7, v9
	v_div_fixup_f32 v4, v6, v5, v146
	ds_write_b32 v3, v4 offset:36864
	s_waitcnt vmcnt(12)
	v_mul_f32_e32 v5, 0xbfb8aa3b, v147
	v_exp_f32_e32 v5, v5
	s_nop 0
	v_add_f32_e32 v5, 1.0, v5
	v_div_scale_f32 v6, s[12:13], v5, v5, v147
	v_rcp_f32_e32 v7, v6
	v_div_scale_f32 v8, vcc, v147, v5, v147
	v_fma_f32 v9, -v6, v7, 1.0
	v_fmac_f32_e32 v7, v9, v7
	v_mul_f32_e32 v9, v8, v7
	v_fma_f32 v10, -v6, v9, v8
	v_fmac_f32_e32 v9, v10, v7
	v_fma_f32 v6, -v6, v9, v8
	v_div_fmas_f32 v6, v6, v7, v9
	v_div_fixup_f32 v4, v6, v5, v147
	ds_write_b32 v3, v4 offset:38912
	s_waitcnt vmcnt(11)
	v_mul_f32_e32 v5, 0xbfb8aa3b, v148
	v_exp_f32_e32 v5, v5
	s_nop 0
	v_add_f32_e32 v5, 1.0, v5
	v_div_scale_f32 v6, s[12:13], v5, v5, v148
	v_rcp_f32_e32 v7, v6
	v_div_scale_f32 v8, vcc, v148, v5, v148
	v_fma_f32 v9, -v6, v7, 1.0
	v_fmac_f32_e32 v7, v9, v7
	v_mul_f32_e32 v9, v8, v7
	v_fma_f32 v10, -v6, v9, v8
	v_fmac_f32_e32 v9, v10, v7
	v_fma_f32 v6, -v6, v9, v8
	v_div_fmas_f32 v6, v6, v7, v9
	v_div_fixup_f32 v4, v6, v5, v148
	ds_write_b32 v3, v4 offset:40960
	s_waitcnt vmcnt(10)
	v_mul_f32_e32 v5, 0xbfb8aa3b, v149
	v_exp_f32_e32 v5, v5
	s_nop 0
	v_add_f32_e32 v5, 1.0, v5
	v_div_scale_f32 v6, s[12:13], v5, v5, v149
	v_rcp_f32_e32 v7, v6
	v_div_scale_f32 v8, vcc, v149, v5, v149
	v_fma_f32 v9, -v6, v7, 1.0
	v_fmac_f32_e32 v7, v9, v7
	v_mul_f32_e32 v9, v8, v7
	v_fma_f32 v10, -v6, v9, v8
	v_fmac_f32_e32 v9, v10, v7
	v_fma_f32 v6, -v6, v9, v8
	v_div_fmas_f32 v6, v6, v7, v9
	v_div_fixup_f32 v4, v6, v5, v149
	ds_write_b32 v3, v4 offset:43008
	s_waitcnt vmcnt(9)
	v_mul_f32_e32 v5, 0xbfb8aa3b, v150
	v_exp_f32_e32 v5, v5
	s_nop 0
	v_add_f32_e32 v5, 1.0, v5
	v_div_scale_f32 v6, s[12:13], v5, v5, v150
	v_rcp_f32_e32 v7, v6
	v_div_scale_f32 v8, vcc, v150, v5, v150
	v_fma_f32 v9, -v6, v7, 1.0
	v_fmac_f32_e32 v7, v9, v7
	v_mul_f32_e32 v9, v8, v7
	v_fma_f32 v10, -v6, v9, v8
	v_fmac_f32_e32 v9, v10, v7
	v_fma_f32 v6, -v6, v9, v8
	v_div_fmas_f32 v6, v6, v7, v9
	v_div_fixup_f32 v4, v6, v5, v150
	ds_write_b32 v3, v4 offset:45056
	s_waitcnt vmcnt(8)
	v_mul_f32_e32 v5, 0xbfb8aa3b, v151
	v_exp_f32_e32 v5, v5
	s_nop 0
	v_add_f32_e32 v5, 1.0, v5
	v_div_scale_f32 v6, s[12:13], v5, v5, v151
	v_rcp_f32_e32 v7, v6
	v_div_scale_f32 v8, vcc, v151, v5, v151
	v_fma_f32 v9, -v6, v7, 1.0
	v_fmac_f32_e32 v7, v9, v7
	v_mul_f32_e32 v9, v8, v7
	v_fma_f32 v10, -v6, v9, v8
	v_fmac_f32_e32 v9, v10, v7
	v_fma_f32 v6, -v6, v9, v8
	v_div_fmas_f32 v6, v6, v7, v9
	v_div_fixup_f32 v4, v6, v5, v151
	ds_write_b32 v3, v4 offset:47104
	s_waitcnt vmcnt(7)
	v_mul_f32_e32 v5, 0xbfb8aa3b, v152
	v_exp_f32_e32 v5, v5
	s_nop 0
	v_add_f32_e32 v5, 1.0, v5
	v_div_scale_f32 v6, s[12:13], v5, v5, v152
	v_rcp_f32_e32 v7, v6
	v_div_scale_f32 v8, vcc, v152, v5, v152
	v_fma_f32 v9, -v6, v7, 1.0
	v_fmac_f32_e32 v7, v9, v7
	v_mul_f32_e32 v9, v8, v7
	v_fma_f32 v10, -v6, v9, v8
	v_fmac_f32_e32 v9, v10, v7
	v_fma_f32 v6, -v6, v9, v8
	v_div_fmas_f32 v6, v6, v7, v9
	v_div_fixup_f32 v4, v6, v5, v152
	ds_write_b32 v3, v4 offset:49152
	s_waitcnt vmcnt(6)
	v_mul_f32_e32 v5, 0xbfb8aa3b, v153
	v_exp_f32_e32 v5, v5
	s_nop 0
	v_add_f32_e32 v5, 1.0, v5
	v_div_scale_f32 v6, s[12:13], v5, v5, v153
	v_rcp_f32_e32 v7, v6
	v_div_scale_f32 v8, vcc, v153, v5, v153
	v_fma_f32 v9, -v6, v7, 1.0
	v_fmac_f32_e32 v7, v9, v7
	v_mul_f32_e32 v9, v8, v7
	v_fma_f32 v10, -v6, v9, v8
	v_fmac_f32_e32 v9, v10, v7
	v_fma_f32 v6, -v6, v9, v8
	v_div_fmas_f32 v6, v6, v7, v9
	v_div_fixup_f32 v4, v6, v5, v153
	ds_write_b32 v3, v4 offset:51200
	s_waitcnt vmcnt(5)
	v_mul_f32_e32 v5, 0xbfb8aa3b, v154
	v_exp_f32_e32 v5, v5
	s_nop 0
	v_add_f32_e32 v5, 1.0, v5
	v_div_scale_f32 v6, s[12:13], v5, v5, v154
	v_rcp_f32_e32 v7, v6
	v_div_scale_f32 v8, vcc, v154, v5, v154
	v_fma_f32 v9, -v6, v7, 1.0
	v_fmac_f32_e32 v7, v9, v7
	v_mul_f32_e32 v9, v8, v7
	v_fma_f32 v10, -v6, v9, v8
	v_fmac_f32_e32 v9, v10, v7
	v_fma_f32 v6, -v6, v9, v8
	v_div_fmas_f32 v6, v6, v7, v9
	v_div_fixup_f32 v4, v6, v5, v154
	ds_write_b32 v3, v4 offset:53248
	s_waitcnt vmcnt(4)
	v_mul_f32_e32 v5, 0xbfb8aa3b, v155
	v_exp_f32_e32 v5, v5
	s_nop 0
	v_add_f32_e32 v5, 1.0, v5
	v_div_scale_f32 v6, s[12:13], v5, v5, v155
	v_rcp_f32_e32 v7, v6
	v_div_scale_f32 v8, vcc, v155, v5, v155
	v_fma_f32 v9, -v6, v7, 1.0
	v_fmac_f32_e32 v7, v9, v7
	v_mul_f32_e32 v9, v8, v7
	v_fma_f32 v10, -v6, v9, v8
	v_fmac_f32_e32 v9, v10, v7
	v_fma_f32 v6, -v6, v9, v8
	v_div_fmas_f32 v6, v6, v7, v9
	v_div_fixup_f32 v4, v6, v5, v155
	ds_write_b32 v3, v4 offset:55296
	s_waitcnt vmcnt(3)
	v_mul_f32_e32 v5, 0xbfb8aa3b, v156
	v_exp_f32_e32 v5, v5
	s_nop 0
	v_add_f32_e32 v5, 1.0, v5
	v_div_scale_f32 v6, s[12:13], v5, v5, v156
	v_rcp_f32_e32 v7, v6
	v_div_scale_f32 v8, vcc, v156, v5, v156
	v_fma_f32 v9, -v6, v7, 1.0
	v_fmac_f32_e32 v7, v9, v7
	v_mul_f32_e32 v9, v8, v7
	v_fma_f32 v10, -v6, v9, v8
	v_fmac_f32_e32 v9, v10, v7
	v_fma_f32 v6, -v6, v9, v8
	v_div_fmas_f32 v6, v6, v7, v9
	v_div_fixup_f32 v4, v6, v5, v156
	ds_write_b32 v3, v4 offset:57344
	s_waitcnt vmcnt(2)
	v_mul_f32_e32 v5, 0xbfb8aa3b, v157
	v_exp_f32_e32 v5, v5
	s_nop 0
	v_add_f32_e32 v5, 1.0, v5
	v_div_scale_f32 v6, s[12:13], v5, v5, v157
	v_rcp_f32_e32 v7, v6
	v_div_scale_f32 v8, vcc, v157, v5, v157
	v_fma_f32 v9, -v6, v7, 1.0
	v_fmac_f32_e32 v7, v9, v7
	v_mul_f32_e32 v9, v8, v7
	v_fma_f32 v10, -v6, v9, v8
	v_fmac_f32_e32 v9, v10, v7
	v_fma_f32 v6, -v6, v9, v8
	v_div_fmas_f32 v6, v6, v7, v9
	v_div_fixup_f32 v4, v6, v5, v157
	ds_write_b32 v3, v4 offset:59392
	s_waitcnt vmcnt(1)
	v_mul_f32_e32 v5, 0xbfb8aa3b, v158
	v_exp_f32_e32 v5, v5
	s_nop 0
	v_add_f32_e32 v5, 1.0, v5
	v_div_scale_f32 v6, s[12:13], v5, v5, v158
	v_rcp_f32_e32 v7, v6
	v_div_scale_f32 v8, vcc, v158, v5, v158
	v_fma_f32 v9, -v6, v7, 1.0
	v_fmac_f32_e32 v7, v9, v7
	v_mul_f32_e32 v9, v8, v7
	v_fma_f32 v10, -v6, v9, v8
	v_fmac_f32_e32 v9, v10, v7
	v_fma_f32 v6, -v6, v9, v8
	v_div_fmas_f32 v6, v6, v7, v9
	v_div_fixup_f32 v4, v6, v5, v158
	ds_write_b32 v3, v4 offset:61440
	s_waitcnt vmcnt(0)
	v_mul_f32_e32 v5, 0xbfb8aa3b, v159
	v_exp_f32_e32 v5, v5
	s_nop 0
	v_add_f32_e32 v5, 1.0, v5
	v_div_scale_f32 v6, s[12:13], v5, v5, v159
	v_rcp_f32_e32 v7, v6
	v_div_scale_f32 v8, vcc, v159, v5, v159
	v_fma_f32 v9, -v6, v7, 1.0
	v_fmac_f32_e32 v7, v9, v7
	v_mul_f32_e32 v9, v8, v7
	v_fma_f32 v10, -v6, v9, v8
	v_fmac_f32_e32 v9, v10, v7
	v_fma_f32 v6, -v6, v9, v8
	v_div_fmas_f32 v6, v6, v7, v9
	v_div_fixup_f32 v4, v6, v5, v159
	ds_write_b32 v3, v4 offset:63488

; #define GAS __attribute__((address_space(1)))
; __device__ __forceinline__ void p0_prologue(Frame& F) {
;     ...
;         for (int item = blockIdx.x; item < 768; item += F.G) {
;             const int l = item / 384, col0 = (item % 384) * 32;
;             f32x4 acc[8];
; #pragma unroll
;             for (int b = 0; b < 8; ++b) acc[b] = (f32x4){0.f, 0.f, 0.f, 0.f};
;             const float* wp = Fw_ada + ((size_t)l * D) * 12288 + col0 + 4 * cg;
; #pragma unroll 4
;             for (int i = 0; i < 32; ++i) { const int k = kq + 64 * i; const f32x4 w4 = *(const GAS f32x4*)(wp + (size_t)k * 12288);
; #pragma unroll
;                 for (int b = 0; b < 8; ++b) { const float cv = cact[b * D + k]; acc[b] += w4 * cv; } }
.LBB0_20:
	s_mul_hi_i32 s0, s15, 0x2aaaaaab
	s_lshr_b32 s1, s0, 31
	s_ashr_i32 s0, s0, 6
	s_add_i32 s16, s0, s1
	s_mul_i32 s0, s16, 0x180
	s_sub_i32 s0, s15, s0
	s_lshl_b32 s0, s0, 5
	s_ashr_i32 s1, s0, 31
	s_mul_i32 s9, s16, 0x6000000
	s_lshl_b64 s[6:7], s[0:1], 2
	s_mul_hi_i32 s8, s16, 0x6000000
	s_add_u32 s0, s9, s6
	s_addc_u32 s1, s8, s7
	v_lshl_add_u64 v[42:43], v[40:41], 0, s[0:1]
	s_mov_b64 s[8:9], 0
	v_mov_b32_e32 v53, v50
	v_mov_b32_e32 v0, 0
	v_mov_b32_e32 v1, v39
	v_mov_b32_e32 v2, 0
	v_mov_b32_e32 v3, v39
	v_mov_b32_e32 v4, 0
	v_mov_b32_e32 v5, v39
	v_mov_b32_e32 v6, 0
	v_mov_b32_e32 v7, v39
	v_mov_b32_e32 v8, 0
	v_mov_b32_e32 v9, v39
	v_mov_b32_e32 v10, 0
	v_mov_b32_e32 v11, v39
	v_mov_b32_e32 v12, 0
	v_mov_b32_e32 v13, v39
	v_mov_b32_e32 v14, 0
	v_mov_b32_e32 v15, v39
	v_mov_b32_e32 v16, 0
	v_mov_b32_e32 v17, v39
	v_mov_b32_e32 v18, 0
	v_mov_b32_e32 v19, v39
	v_mov_b32_e32 v20, 0
	v_mov_b32_e32 v21, v39
	v_mov_b32_e32 v22, 0
	v_mov_b32_e32 v23, v39
	v_mov_b32_e32 v24, 0
	v_mov_b32_e32 v25, v39
	v_mov_b32_e32 v26, 0
	v_mov_b32_e32 v27, v39
	v_mov_b32_e32 v28, 0
	v_mov_b32_e32 v29, v39
	v_mov_b32_e32 v30, 0
	v_mov_b32_e32 v31, v39
	v_lshl_add_u64 v[48:49], v[42:43], 0, s[8:9]
	v_add_co_u32_e64 v98, s[0:1], s12, v48
	s_nop 1
	v_addc_co_u32_e64 v99, s[0:1], 0, v49, s[0:1]
	v_add_co_u32_e64 v100, s[0:1], s13, v48
	s_nop 1
	v_addc_co_u32_e64 v101, s[0:1], 0, v49, s[0:1]
	global_load_dwordx4 v[54:57], v[48:49], off
	global_load_dwordx4 v[58:61], v[98:99], off
	global_load_dwordx4 v[62:65], v[100:101], off
	v_add_co_u32_e64 v48, s[0:1], s14, v48
	s_nop 1
	v_addc_co_u32_e64 v49, s[0:1], 0, v49, s[0:1]
	global_load_dwordx4 v[66:69], v[48:49], off
	s_add_u32 s8, s8, 0xc00000
	s_addc_u32 s9, s9, 0
.LBB0_21:
	v_lshl_add_u64 v[48:49], v[42:43], 0, s[8:9]
	v_add_co_u32_e64 v98, s[0:1], s12, v48
	s_nop 1
	v_addc_co_u32_e64 v99, s[0:1], 0, v49, s[0:1]
	v_add_co_u32_e64 v100, s[0:1], s13, v48
	s_nop 1
	v_addc_co_u32_e64 v101, s[0:1], 0, v49, s[0:1]
	global_load_dwordx4 v[128:131], v[48:49], off
	global_load_dwordx4 v[132:135], v[98:99], off
	global_load_dwordx4 v[136:139], v[100:101], off
	v_add_co_u32_e64 v48, s[0:1], s14, v48
	s_nop 1
	v_addc_co_u32_e64 v49, s[0:1], 0, v49, s[0:1]
	global_load_dwordx4 v[140:143], v[48:49], off
	s_add_u32 s8, s8, 0xc00000
	s_addc_u32 s9, s9, 0
	ds_read2st64_b32 v[44:45], v53 offset1:1
	ds_read2st64_b32 v[46:47], v53 offset0:32 offset1:33
	ds_read2st64_b32 v[70:71], v53 offset0:34 offset1:35
	ds_read2st64_b32 v[72:73], v53 offset0:2 offset1:3
	ds_read2st64_b32 v[74:75], v53 offset0:64 offset1:65
	ds_read2st64_b32 v[76:77], v53 offset0:98 offset1:99
	ds_read2st64_b32 v[78:79], v53 offset0:66 offset1:67
	ds_read2st64_b32 v[80:81], v53 offset0:96 offset1:97
	ds_read2st64_b32 v[82:83], v53 offset0:128 offset1:129
	ds_read2st64_b32 v[84:85], v53 offset0:162 offset1:163
	ds_read2st64_b32 v[86:87], v53 offset0:130 offset1:131
	ds_read2st64_b32 v[88:89], v53 offset0:160 offset1:161
	ds_read2st64_b32 v[90:91], v53 offset0:192 offset1:193
	ds_read2st64_b32 v[92:93], v53 offset0:226 offset1:227
	ds_read2st64_b32 v[94:95], v53 offset0:194 offset1:195
	ds_read2st64_b32 v[96:97], v53 offset0:224 offset1:225
	s_waitcnt lgkmcnt(0)
	v_mov_b32_e32 v102, v81
	v_mov_b32_e32 v104, v83
	v_mov_b32_e32 v48, v45
	v_mov_b32_e32 v98, v47
	v_mov_b32_e32 v100, v75
	v_mov_b32_e32 v106, v89
	v_mov_b32_e32 v108, v91
	v_mov_b32_e32 v110, v97
	v_mov_b32_e32 v112, v73
	v_mov_b32_e32 v114, v71
	v_mov_b32_e32 v116, v79
	v_mov_b32_e32 v118, v77
	v_mov_b32_e32 v120, v87
	v_mov_b32_e32 v122, v85
	v_mov_b32_e32 v124, v95
	v_mov_b32_e32 v126, v93
	v_add_u32_e32 v53, 0x400, v53
	s_waitcnt vmcnt(7)
	v_pk_fma_f32 v[28:29], v[54:55], v[44:45], v[28:29] op_sel_hi:[1,0,1]
	v_pk_fma_f32 v[30:31], v[56:57], v[44:45], v[30:31] op_sel_hi:[1,0,1]
	v_pk_fma_f32 v[24:25], v[54:55], v[46:47], v[24:25] op_sel_hi:[1,0,1]
	v_pk_fma_f32 v[26:27], v[56:57], v[46:47], v[26:27] op_sel_hi:[1,0,1]
	v_pk_fma_f32 v[20:21], v[54:55], v[74:75], v[20:21] op_sel_hi:[1,0,1]
	v_pk_fma_f32 v[22:23], v[56:57], v[74:75], v[22:23] op_sel_hi:[1,0,1]
	v_pk_fma_f32 v[16:17], v[54:55], v[80:81], v[16:17] op_sel_hi:[1,0,1]
	v_pk_fma_f32 v[18:19], v[56:57], v[80:81], v[18:19] op_sel_hi:[1,0,1]
	v_pk_fma_f32 v[12:13], v[54:55], v[82:83], v[12:13] op_sel_hi:[1,0,1]
	v_pk_fma_f32 v[14:15], v[56:57], v[82:83], v[14:15] op_sel_hi:[1,0,1]
	v_pk_fma_f32 v[8:9], v[54:55], v[88:89], v[8:9] op_sel_hi:[1,0,1]
	v_pk_fma_f32 v[10:11], v[56:57], v[88:89], v[10:11] op_sel_hi:[1,0,1]
	v_pk_fma_f32 v[4:5], v[54:55], v[90:91], v[4:5] op_sel_hi:[1,0,1]
	v_pk_fma_f32 v[6:7], v[56:57], v[90:91], v[6:7] op_sel_hi:[1,0,1]
	v_pk_fma_f32 v[0:1], v[54:55], v[96:97], v[0:1] op_sel_hi:[1,0,1]
	v_pk_fma_f32 v[2:3], v[56:57], v[96:97], v[2:3] op_sel_hi:[1,0,1]
	s_waitcnt vmcnt(6)
	v_pk_fma_f32 v[28:29], v[58:59], v[48:49], v[28:29] op_sel_hi:[1,0,1]
	v_pk_fma_f32 v[30:31], v[60:61], v[48:49], v[30:31] op_sel_hi:[1,0,1]
	v_pk_fma_f32 v[24:25], v[58:59], v[98:99], v[24:25] op_sel_hi:[1,0,1]
	v_pk_fma_f32 v[26:27], v[60:61], v[98:99], v[26:27] op_sel_hi:[1,0,1]
	v_pk_fma_f32 v[20:21], v[58:59], v[100:101], v[20:21] op_sel_hi:[1,0,1]
	v_pk_fma_f32 v[22:23], v[60:61], v[100:101], v[22:23] op_sel_hi:[1,0,1]
	v_pk_fma_f32 v[16:17], v[58:59], v[102:103], v[16:17] op_sel_hi:[1,0,1]
	v_pk_fma_f32 v[18:19], v[60:61], v[102:103], v[18:19] op_sel_hi:[1,0,1]
	v_pk_fma_f32 v[12:13], v[58:59], v[104:105], v[12:13] op_sel_hi:[1,0,1]
	v_pk_fma_f32 v[14:15], v[60:61], v[104:105], v[14:15] op_sel_hi:[1,0,1]
	v_pk_fma_f32 v[8:9], v[58:59], v[106:107], v[8:9] op_sel_hi:[1,0,1]
	v_pk_fma_f32 v[10:11], v[60:61], v[106:107], v[10:11] op_sel_hi:[1,0,1]
	v_pk_fma_f32 v[4:5], v[58:59], v[108:109], v[4:5] op_sel_hi:[1,0,1]
	v_pk_fma_f32 v[6:7], v[60:61], v[108:109], v[6:7] op_sel_hi:[1,0,1]
	v_pk_fma_f32 v[0:1], v[58:59], v[110:111], v[0:1] op_sel_hi:[1,0,1]
	v_pk_fma_f32 v[2:3], v[60:61], v[110:111], v[2:3] op_sel_hi:[1,0,1]
	s_waitcnt vmcnt(5)
; #define GAS __attribute__((address_space(1)))
; __device__ __forceinline__ void p0_prologue(Frame& F) {
;     ...
;             for (int i = 0; i < 32; ++i) { const int k = kq + 64 * i; const f32x4 w4 = *(const GAS f32x4*)(wp + (size_t)k * 12288);
; #pragma unroll
;                 for (int b = 0; b < 8; ++b) { const float cv = cact[b * D + k]; acc[b] += w4 * cv; } }
	v_pk_fma_f32 v[30:31], v[64:65], v[72:73], v[30:31] op_sel_hi:[1,0,1]
	v_pk_fma_f32 v[28:29], v[62:63], v[72:73], v[28:29] op_sel_hi:[1,0,1]
	v_pk_fma_f32 v[26:27], v[64:65], v[70:71], v[26:27] op_sel_hi:[1,0,1]
	v_pk_fma_f32 v[24:25], v[62:63], v[70:71], v[24:25] op_sel_hi:[1,0,1]
	v_pk_fma_f32 v[22:23], v[64:65], v[78:79], v[22:23] op_sel_hi:[1,0,1]
	v_pk_fma_f32 v[20:21], v[62:63], v[78:79], v[20:21] op_sel_hi:[1,0,1]
	v_pk_fma_f32 v[18:19], v[64:65], v[76:77], v[18:19] op_sel_hi:[1,0,1]
	v_pk_fma_f32 v[16:17], v[62:63], v[76:77], v[16:17] op_sel_hi:[1,0,1]
	v_pk_fma_f32 v[14:15], v[64:65], v[86:87], v[14:15] op_sel_hi:[1,0,1]
	v_pk_fma_f32 v[12:13], v[62:63], v[86:87], v[12:13] op_sel_hi:[1,0,1]
	v_pk_fma_f32 v[10:11], v[64:65], v[84:85], v[10:11] op_sel_hi:[1,0,1]
	v_pk_fma_f32 v[8:9], v[62:63], v[84:85], v[8:9] op_sel_hi:[1,0,1]
	v_pk_fma_f32 v[6:7], v[64:65], v[94:95], v[6:7] op_sel_hi:[1,0,1]
	v_pk_fma_f32 v[4:5], v[62:63], v[94:95], v[4:5] op_sel_hi:[1,0,1]
	v_pk_fma_f32 v[2:3], v[64:65], v[92:93], v[2:3] op_sel_hi:[1,0,1]
	v_pk_fma_f32 v[0:1], v[62:63], v[92:93], v[0:1] op_sel_hi:[1,0,1]
	s_waitcnt vmcnt(4)
	v_pk_fma_f32 v[30:31], v[68:69], v[112:113], v[30:31] op_sel_hi:[1,0,1]
	v_pk_fma_f32 v[28:29], v[66:67], v[112:113], v[28:29] op_sel_hi:[1,0,1]
	v_pk_fma_f32 v[26:27], v[68:69], v[114:115], v[26:27] op_sel_hi:[1,0,1]
	v_pk_fma_f32 v[24:25], v[66:67], v[114:115], v[24:25] op_sel_hi:[1,0,1]
	v_pk_fma_f32 v[22:23], v[68:69], v[116:117], v[22:23] op_sel_hi:[1,0,1]
	v_pk_fma_f32 v[20:21], v[66:67], v[116:117], v[20:21] op_sel_hi:[1,0,1]
	v_pk_fma_f32 v[18:19], v[68:69], v[118:119], v[18:19] op_sel_hi:[1,0,1]
	v_pk_fma_f32 v[16:17], v[66:67], v[118:119], v[16:17] op_sel_hi:[1,0,1]
	v_pk_fma_f32 v[14:15], v[68:69], v[120:121], v[14:15] op_sel_hi:[1,0,1]
	v_pk_fma_f32 v[12:13], v[66:67], v[120:121], v[12:13] op_sel_hi:[1,0,1]
	v_pk_fma_f32 v[10:11], v[68:69], v[122:123], v[10:11] op_sel_hi:[1,0,1]
	v_pk_fma_f32 v[8:9], v[66:67], v[122:123], v[8:9] op_sel_hi:[1,0,1]
	v_pk_fma_f32 v[6:7], v[68:69], v[124:125], v[6:7] op_sel_hi:[1,0,1]
	v_pk_fma_f32 v[4:5], v[66:67], v[124:125], v[4:5] op_sel_hi:[1,0,1]
	v_pk_fma_f32 v[2:3], v[68:69], v[126:127], v[2:3] op_sel_hi:[1,0,1]
	v_pk_fma_f32 v[0:1], v[66:67], v[126:127], v[0:1] op_sel_hi:[1,0,1]
	s_cmp_eq_u32 s8, 0x6000000
	s_cbranch_scc1 .Lgemv_lastB
	v_lshl_add_u64 v[48:49], v[42:43], 0, s[8:9]
	v_add_co_u32_e64 v98, s[0:1], s12, v48
	s_nop 1
	v_addc_co_u32_e64 v99, s[0:1], 0, v49, s[0:1]
	v_add_co_u32_e64 v100, s[0:1], s13, v48
	s_nop 1
	v_addc_co_u32_e64 v101, s[0:1], 0, v49, s[0:1]
	global_load_dwordx4 v[54:57], v[48:49], off
	global_load_dwordx4 v[58:61], v[98:99], off
	global_load_dwordx4 v[62:65], v[100:101], off
	v_add_co_u32_e64 v48, s[0:1], s14, v48
	s_nop 1
	v_addc_co_u32_e64 v49, s[0:1], 0, v49, s[0:1]
	global_load_dwordx4 v[66:69], v[48:49], off
	s_add_u32 s8, s8, 0xc00000
	s_addc_u32 s9, s9, 0
	ds_read2st64_b32 v[44:45], v53 offset1:1
	ds_read2st64_b32 v[46:47], v53 offset0:32 offset1:33
	ds_read2st64_b32 v[70:71], v53 offset0:34 offset1:35
	ds_read2st64_b32 v[72:73], v53 offset0:2 offset1:3
	ds_read2st64_b32 v[74:75], v53 offset0:64 offset1:65
	ds_read2st64_b32 v[76:77], v53 offset0:98 offset1:99
	ds_read2st64_b32 v[78:79], v53 offset0:66 offset1:67
	ds_read2st64_b32 v[80:81], v53 offset0:96 offset1:97
	ds_read2st64_b32 v[82:83], v53 offset0:128 offset1:129
	ds_read2st64_b32 v[84:85], v53 offset0:162 offset1:163
	ds_read2st64_b32 v[86:87], v53 offset0:130 offset1:131
	ds_read2st64_b32 v[88:89], v53 offset0:160 offset1:161
	ds_read2st64_b32 v[90:91], v53 offset0:192 offset1:193
	ds_read2st64_b32 v[92:93], v53 offset0:226 offset1:227
	ds_read2st64_b32 v[94:95], v53 offset0:194 offset1:195
	ds_read2st64_b32 v[96:97], v53 offset0:224 offset1:225
	s_waitcnt lgkmcnt(0)
	v_mov_b32_e32 v102, v81
	v_mov_b32_e32 v104, v83
	v_mov_b32_e32 v48, v45
	v_mov_b32_e32 v98, v47
	v_mov_b32_e32 v100, v75
	v_mov_b32_e32 v106, v89
	v_mov_b32_e32 v108, v91
	v_mov_b32_e32 v110, v97
	v_mov_b32_e32 v112, v73
	v_mov_b32_e32 v114, v71
	v_mov_b32_e32 v116, v79
	v_mov_b32_e32 v118, v77
	v_mov_b32_e32 v120, v87
	v_mov_b32_e32 v122, v85
	v_mov_b32_e32 v124, v95
	v_mov_b32_e32 v126, v93
	v_add_u32_e32 v53, 0x400, v53
	s_waitcnt vmcnt(7)
	v_pk_fma_f32 v[28:29], v[128:129], v[44:45], v[28:29] op_sel_hi:[1,0,1]
	v_pk_fma_f32 v[30:31], v[130:131], v[44:45], v[30:31] op_sel_hi:[1,0,1]
	v_pk_fma_f32 v[24:25], v[128:129], v[46:47], v[24:25] op_sel_hi:[1,0,1]
	v_pk_fma_f32 v[26:27], v[130:131], v[46:47], v[26:27] op_sel_hi:[1,0,1]
	v_pk_fma_f32 v[20:21], v[128:129], v[74:75], v[20:21] op_sel_hi:[1,0,1]
	v_pk_fma_f32 v[22:23], v[130:131], v[74:75], v[22:23] op_sel_hi:[1,0,1]
	v_pk_fma_f32 v[16:17], v[128:129], v[80:81], v[16:17] op_sel_hi:[1,0,1]
	v_pk_fma_f32 v[18:19], v[130:131], v[80:81], v[18:19] op_sel_hi:[1,0,1]
	v_pk_fma_f32 v[12:13], v[128:129], v[82:83], v[12:13] op_sel_hi:[1,0,1]
	v_pk_fma_f32 v[14:15], v[130:131], v[82:83], v[14:15] op_sel_hi:[1,0,1]
	v_pk_fma_f32 v[8:9], v[128:129], v[88:89], v[8:9] op_sel_hi:[1,0,1]
	v_pk_fma_f32 v[10:11], v[130:131], v[88:89], v[10:11] op_sel_hi:[1,0,1]
	v_pk_fma_f32 v[4:5], v[128:129], v[90:91], v[4:5] op_sel_hi:[1,0,1]
	v_pk_fma_f32 v[6:7], v[130:131], v[90:91], v[6:7] op_sel_hi:[1,0,1]
	v_pk_fma_f32 v[0:1], v[128:129], v[96:97], v[0:1] op_sel_hi:[1,0,1]
	v_pk_fma_f32 v[2:3], v[130:131], v[96:97], v[2:3] op_sel_hi:[1,0,1]
	s_waitcnt vmcnt(6)
; #define GAS __attribute__((address_space(1)))
; __device__ __forceinline__ void p0_prologue(Frame& F) {
;     ...
;             for (int i = 0; i < 32; ++i) { const int k = kq + 64 * i; const f32x4 w4 = *(const GAS f32x4*)(wp + (size_t)k * 12288);
; #pragma unroll
;                 for (int b = 0; b < 8; ++b) { const float cv = cact[b * D + k]; acc[b] += w4 * cv; } }
	v_pk_fma_f32 v[28:29], v[132:133], v[48:49], v[28:29] op_sel_hi:[1,0,1]
	v_pk_fma_f32 v[30:31], v[134:135], v[48:49], v[30:31] op_sel_hi:[1,0,1]
	v_pk_fma_f32 v[24:25], v[132:133], v[98:99], v[24:25] op_sel_hi:[1,0,1]
	v_pk_fma_f32 v[26:27], v[134:135], v[98:99], v[26:27] op_sel_hi:[1,0,1]
	v_pk_fma_f32 v[20:21], v[132:133], v[100:101], v[20:21] op_sel_hi:[1,0,1]
	v_pk_fma_f32 v[22:23], v[134:135], v[100:101], v[22:23] op_sel_hi:[1,0,1]
	v_pk_fma_f32 v[16:17], v[132:133], v[102:103], v[16:17] op_sel_hi:[1,0,1]
	v_pk_fma_f32 v[18:19], v[134:135], v[102:103], v[18:19] op_sel_hi:[1,0,1]
	v_pk_fma_f32 v[12:13], v[132:133], v[104:105], v[12:13] op_sel_hi:[1,0,1]
	v_pk_fma_f32 v[14:15], v[134:135], v[104:105], v[14:15] op_sel_hi:[1,0,1]
	v_pk_fma_f32 v[8:9], v[132:133], v[106:107], v[8:9] op_sel_hi:[1,0,1]
	v_pk_fma_f32 v[10:11], v[134:135], v[106:107], v[10:11] op_sel_hi:[1,0,1]
	v_pk_fma_f32 v[4:5], v[132:133], v[108:109], v[4:5] op_sel_hi:[1,0,1]
	v_pk_fma_f32 v[6:7], v[134:135], v[108:109], v[6:7] op_sel_hi:[1,0,1]
	v_pk_fma_f32 v[0:1], v[132:133], v[110:111], v[0:1] op_sel_hi:[1,0,1]
	v_pk_fma_f32 v[2:3], v[134:135], v[110:111], v[2:3] op_sel_hi:[1,0,1]
	s_waitcnt vmcnt(5)
	v_pk_fma_f32 v[30:31], v[138:139], v[72:73], v[30:31] op_sel_hi:[1,0,1]
	v_pk_fma_f32 v[28:29], v[136:137], v[72:73], v[28:29] op_sel_hi:[1,0,1]
	v_pk_fma_f32 v[26:27], v[138:139], v[70:71], v[26:27] op_sel_hi:[1,0,1]
	v_pk_fma_f32 v[24:25], v[136:137], v[70:71], v[24:25] op_sel_hi:[1,0,1]
	v_pk_fma_f32 v[22:23], v[138:139], v[78:79], v[22:23] op_sel_hi:[1,0,1]
	v_pk_fma_f32 v[20:21], v[136:137], v[78:79], v[20:21] op_sel_hi:[1,0,1]
	v_pk_fma_f32 v[18:19], v[138:139], v[76:77], v[18:19] op_sel_hi:[1,0,1]
	v_pk_fma_f32 v[16:17], v[136:137], v[76:77], v[16:17] op_sel_hi:[1,0,1]
	v_pk_fma_f32 v[14:15], v[138:139], v[86:87], v[14:15] op_sel_hi:[1,0,1]
	v_pk_fma_f32 v[12:13], v[136:137], v[86:87], v[12:13] op_sel_hi:[1,0,1]
	v_pk_fma_f32 v[10:11], v[138:139], v[84:85], v[10:11] op_sel_hi:[1,0,1]
	v_pk_fma_f32 v[8:9], v[136:137], v[84:85], v[8:9] op_sel_hi:[1,0,1]
	v_pk_fma_f32 v[6:7], v[138:139], v[94:95], v[6:7] op_sel_hi:[1,0,1]
	v_pk_fma_f32 v[4:5], v[136:137], v[94:95], v[4:5] op_sel_hi:[1,0,1]
	v_pk_fma_f32 v[2:3], v[138:139], v[92:93], v[2:3] op_sel_hi:[1,0,1]
	v_pk_fma_f32 v[0:1], v[136:137], v[92:93], v[0:1] op_sel_hi:[1,0,1]
	s_waitcnt vmcnt(4)
	v_pk_fma_f32 v[30:31], v[142:143], v[112:113], v[30:31] op_sel_hi:[1,0,1]
	v_pk_fma_f32 v[28:29], v[140:141], v[112:113], v[28:29] op_sel_hi:[1,0,1]
	v_pk_fma_f32 v[26:27], v[142:143], v[114:115], v[26:27] op_sel_hi:[1,0,1]
	v_pk_fma_f32 v[24:25], v[140:141], v[114:115], v[24:25] op_sel_hi:[1,0,1]
	v_pk_fma_f32 v[22:23], v[142:143], v[116:117], v[22:23] op_sel_hi:[1,0,1]
	v_pk_fma_f32 v[20:21], v[140:141], v[116:117], v[20:21] op_sel_hi:[1,0,1]
	v_pk_fma_f32 v[18:19], v[142:143], v[118:119], v[18:19] op_sel_hi:[1,0,1]
	v_pk_fma_f32 v[16:17], v[140:141], v[118:119], v[16:17] op_sel_hi:[1,0,1]
	v_pk_fma_f32 v[14:15], v[142:143], v[120:121], v[14:15] op_sel_hi:[1,0,1]
	v_pk_fma_f32 v[12:13], v[140:141], v[120:121], v[12:13] op_sel_hi:[1,0,1]
	v_pk_fma_f32 v[10:11], v[142:143], v[122:123], v[10:11] op_sel_hi:[1,0,1]
	v_pk_fma_f32 v[8:9], v[140:141], v[122:123], v[8:9] op_sel_hi:[1,0,1]
	v_pk_fma_f32 v[6:7], v[142:143], v[124:125], v[6:7] op_sel_hi:[1,0,1]
	v_pk_fma_f32 v[4:5], v[140:141], v[124:125], v[4:5] op_sel_hi:[1,0,1]
	v_pk_fma_f32 v[2:3], v[142:143], v[126:127], v[2:3] op_sel_hi:[1,0,1]
	v_pk_fma_f32 v[0:1], v[140:141], v[126:127], v[0:1] op_sel_hi:[1,0,1]
	s_branch .LBB0_21
.Lgemv_lastB:
	ds_read2st64_b32 v[44:45], v53 offset1:1
	ds_read2st64_b32 v[46:47], v53 offset0:32 offset1:33
	ds_read2st64_b32 v[70:71], v53 offset0:34 offset1:35
	ds_read2st64_b32 v[72:73], v53 offset0:2 offset1:3
	ds_read2st64_b32 v[74:75], v53 offset0:64 offset1:65
	ds_read2st64_b32 v[76:77], v53 offset0:98 offset1:99
	ds_read2st64_b32 v[78:79], v53 offset0:66 offset1:67
	ds_read2st64_b32 v[80:81], v53 offset0:96 offset1:97
	ds_read2st64_b32 v[82:83], v53 offset0:128 offset1:129
	ds_read2st64_b32 v[84:85], v53 offset0:162 offset1:163
	ds_read2st64_b32 v[86:87], v53 offset0:130 offset1:131
	ds_read2st64_b32 v[88:89], v53 offset0:160 offset1:161
	ds_read2st64_b32 v[90:91], v53 offset0:192 offset1:193
	ds_read2st64_b32 v[92:93], v53 offset0:226 offset1:227
	ds_read2st64_b32 v[94:95], v53 offset0:194 offset1:195
	ds_read2st64_b32 v[96:97], v53 offset0:224 offset1:225
	s_waitcnt lgkmcnt(0)
	v_mov_b32_e32 v102, v81
	v_mov_b32_e32 v104, v83
	v_mov_b32_e32 v48, v45
	v_mov_b32_e32 v98, v47
	v_mov_b32_e32 v100, v75
	v_mov_b32_e32 v106, v89
	v_mov_b32_e32 v108, v91
	v_mov_b32_e32 v110, v97
	v_mov_b32_e32 v112, v73
	v_mov_b32_e32 v114, v71
	v_mov_b32_e32 v116, v79
	v_mov_b32_e32 v118, v77
	v_mov_b32_e32 v120, v87
	v_mov_b32_e32 v122, v85
	v_mov_b32_e32 v124, v95
	v_mov_b32_e32 v126, v93
	v_add_u32_e32 v53, 0x400, v53
	s_waitcnt vmcnt(3)
	v_pk_fma_f32 v[28:29], v[128:129], v[44:45], v[28:29] op_sel_hi:[1,0,1]
	v_pk_fma_f32 v[30:31], v[130:131], v[44:45], v[30:31] op_sel_hi:[1,0,1]
	v_pk_fma_f32 v[24:25], v[128:129], v[46:47], v[24:25] op_sel_hi:[1,0,1]
	v_pk_fma_f32 v[26:27], v[130:131], v[46:47], v[26:27] op_sel_hi:[1,0,1]
	v_pk_fma_f32 v[20:21], v[128:129], v[74:75], v[20:21] op_sel_hi:[1,0,1]
	v_pk_fma_f32 v[22:23], v[130:131], v[74:75], v[22:23] op_sel_hi:[1,0,1]
	v_pk_fma_f32 v[16:17], v[128:129], v[80:81], v[16:17] op_sel_hi:[1,0,1]
	v_pk_fma_f32 v[18:19], v[130:131], v[80:81], v[18:19] op_sel_hi:[1,0,1]
	v_pk_fma_f32 v[12:13], v[128:129], v[82:83], v[12:13] op_sel_hi:[1,0,1]
	v_pk_fma_f32 v[14:15], v[130:131], v[82:83], v[14:15] op_sel_hi:[1,0,1]
	v_pk_fma_f32 v[8:9], v[128:129], v[88:89], v[8:9] op_sel_hi:[1,0,1]
	v_pk_fma_f32 v[10:11], v[130:131], v[88:89], v[10:11] op_sel_hi:[1,0,1]
	v_pk_fma_f32 v[4:5], v[128:129], v[90:91], v[4:5] op_sel_hi:[1,0,1]
	v_pk_fma_f32 v[6:7], v[130:131], v[90:91], v[6:7] op_sel_hi:[1,0,1]
	v_pk_fma_f32 v[0:1], v[128:129], v[96:97], v[0:1] op_sel_hi:[1,0,1]
	v_pk_fma_f32 v[2:3], v[130:131], v[96:97], v[2:3] op_sel_hi:[1,0,1]
	s_waitcnt vmcnt(2)
; #define GAS __attribute__((address_space(1)))
; #define LAS __attribute__((address_space(3)))
; __device__ __forceinline__ void p0_prologue(Frame& F) {
;     ...
;             for (int i = 0; i < 32; ++i) { const int k = kq + 64 * i; const f32x4 w4 = *(const GAS f32x4*)(wp + (size_t)k * 12288);
; #pragma unroll
;                 for (int b = 0; b < 8; ++b) { const float cv = cact[b * D + k]; acc[b] += w4 * cv; } }
; #pragma unroll
;             for (int b = 0; b < 8; ++b) *(LAS f32x4*)(part + (kq * 8 + b) * 32 + 4 * cg) = acc[b];
;             __syncthreads();
;             if (F.tid < 256) { const int b = F.tid >> 5, col = F.tid & 31; float s = 0.f;
;                 for (int q = 0; q < 64; ++q) s += part[(q * 8 + b) * 32 + col];
;                 mod[((size_t)l * 8 + b) * 12288 + col0 + col] = s + Fb_ada[(size_t)l * 12288 + col0 + col]; }
;             __syncthreads();
	v_pk_fma_f32 v[28:29], v[132:133], v[48:49], v[28:29] op_sel_hi:[1,0,1]
	v_pk_fma_f32 v[30:31], v[134:135], v[48:49], v[30:31] op_sel_hi:[1,0,1]
	v_pk_fma_f32 v[24:25], v[132:133], v[98:99], v[24:25] op_sel_hi:[1,0,1]
	v_pk_fma_f32 v[26:27], v[134:135], v[98:99], v[26:27] op_sel_hi:[1,0,1]
	v_pk_fma_f32 v[20:21], v[132:133], v[100:101], v[20:21] op_sel_hi:[1,0,1]
	v_pk_fma_f32 v[22:23], v[134:135], v[100:101], v[22:23] op_sel_hi:[1,0,1]
	v_pk_fma_f32 v[16:17], v[132:133], v[102:103], v[16:17] op_sel_hi:[1,0,1]
	v_pk_fma_f32 v[18:19], v[134:135], v[102:103], v[18:19] op_sel_hi:[1,0,1]
	v_pk_fma_f32 v[12:13], v[132:133], v[104:105], v[12:13] op_sel_hi:[1,0,1]
	v_pk_fma_f32 v[14:15], v[134:135], v[104:105], v[14:15] op_sel_hi:[1,0,1]
	v_pk_fma_f32 v[8:9], v[132:133], v[106:107], v[8:9] op_sel_hi:[1,0,1]
	v_pk_fma_f32 v[10:11], v[134:135], v[106:107], v[10:11] op_sel_hi:[1,0,1]
	v_pk_fma_f32 v[4:5], v[132:133], v[108:109], v[4:5] op_sel_hi:[1,0,1]
	v_pk_fma_f32 v[6:7], v[134:135], v[108:109], v[6:7] op_sel_hi:[1,0,1]
	v_pk_fma_f32 v[0:1], v[132:133], v[110:111], v[0:1] op_sel_hi:[1,0,1]
	v_pk_fma_f32 v[2:3], v[134:135], v[110:111], v[2:3] op_sel_hi:[1,0,1]
	s_waitcnt vmcnt(1)
	v_pk_fma_f32 v[30:31], v[138:139], v[72:73], v[30:31] op_sel_hi:[1,0,1]
	v_pk_fma_f32 v[28:29], v[136:137], v[72:73], v[28:29] op_sel_hi:[1,0,1]
	v_pk_fma_f32 v[26:27], v[138:139], v[70:71], v[26:27] op_sel_hi:[1,0,1]
	v_pk_fma_f32 v[24:25], v[136:137], v[70:71], v[24:25] op_sel_hi:[1,0,1]
	v_pk_fma_f32 v[22:23], v[138:139], v[78:79], v[22:23] op_sel_hi:[1,0,1]
	v_pk_fma_f32 v[20:21], v[136:137], v[78:79], v[20:21] op_sel_hi:[1,0,1]
	v_pk_fma_f32 v[18:19], v[138:139], v[76:77], v[18:19] op_sel_hi:[1,0,1]
	v_pk_fma_f32 v[16:17], v[136:137], v[76:77], v[16:17] op_sel_hi:[1,0,1]
	v_pk_fma_f32 v[14:15], v[138:139], v[86:87], v[14:15] op_sel_hi:[1,0,1]
	v_pk_fma_f32 v[12:13], v[136:137], v[86:87], v[12:13] op_sel_hi:[1,0,1]
	v_pk_fma_f32 v[10:11], v[138:139], v[84:85], v[10:11] op_sel_hi:[1,0,1]
	v_pk_fma_f32 v[8:9], v[136:137], v[84:85], v[8:9] op_sel_hi:[1,0,1]
	v_pk_fma_f32 v[6:7], v[138:139], v[94:95], v[6:7] op_sel_hi:[1,0,1]
	v_pk_fma_f32 v[4:5], v[136:137], v[94:95], v[4:5] op_sel_hi:[1,0,1]
	v_pk_fma_f32 v[2:3], v[138:139], v[92:93], v[2:3] op_sel_hi:[1,0,1]
	v_pk_fma_f32 v[0:1], v[136:137], v[92:93], v[0:1] op_sel_hi:[1,0,1]
	s_waitcnt vmcnt(0)
	v_pk_fma_f32 v[30:31], v[142:143], v[112:113], v[30:31] op_sel_hi:[1,0,1]
	v_pk_fma_f32 v[28:29], v[140:141], v[112:113], v[28:29] op_sel_hi:[1,0,1]
	v_pk_fma_f32 v[26:27], v[142:143], v[114:115], v[26:27] op_sel_hi:[1,0,1]
	v_pk_fma_f32 v[24:25], v[140:141], v[114:115], v[24:25] op_sel_hi:[1,0,1]
	v_pk_fma_f32 v[22:23], v[142:143], v[116:117], v[22:23] op_sel_hi:[1,0,1]
	v_pk_fma_f32 v[20:21], v[140:141], v[116:117], v[20:21] op_sel_hi:[1,0,1]
	v_pk_fma_f32 v[18:19], v[142:143], v[118:119], v[18:19] op_sel_hi:[1,0,1]
	v_pk_fma_f32 v[16:17], v[140:141], v[118:119], v[16:17] op_sel_hi:[1,0,1]
	v_pk_fma_f32 v[14:15], v[142:143], v[120:121], v[14:15] op_sel_hi:[1,0,1]
	v_pk_fma_f32 v[12:13], v[140:141], v[120:121], v[12:13] op_sel_hi:[1,0,1]
	v_pk_fma_f32 v[10:11], v[142:143], v[122:123], v[10:11] op_sel_hi:[1,0,1]
	v_pk_fma_f32 v[8:9], v[140:141], v[122:123], v[8:9] op_sel_hi:[1,0,1]
	v_pk_fma_f32 v[6:7], v[142:143], v[124:125], v[6:7] op_sel_hi:[1,0,1]
	v_pk_fma_f32 v[4:5], v[140:141], v[124:125], v[4:5] op_sel_hi:[1,0,1]
	v_pk_fma_f32 v[2:3], v[142:143], v[126:127], v[2:3] op_sel_hi:[1,0,1]
	v_pk_fma_f32 v[0:1], v[140:141], v[126:127], v[0:1] op_sel_hi:[1,0,1]
	ds_write_b128 v51, v[28:31]
	ds_write_b128 v51, v[24:27] offset:128
	ds_write_b128 v51, v[20:23] offset:256
	ds_write_b128 v51, v[16:19] offset:384
	ds_write_b128 v51, v[12:15] offset:512
	ds_write_b128 v51, v[8:11] offset:640
	ds_write_b128 v51, v[4:7] offset:768
	ds_write_b128 v52, v[0:3]
	s_waitcnt lgkmcnt(0)
	s_barrier
	s_and_saveexec_b64 s[0:1], vcc
	s_cbranch_execz .LBB0_19
; __device__ __forceinline__ void p0_prologue(Frame& F) {
;     ...
;             if (F.tid < 256) { const int b = F.tid >> 5, col = F.tid & 31; float s = 0.f;
;                 for (int q = 0; q < 64; ++q) s += part[(q * 8 + b) * 32 + col];
;                 mod[((size_t)l * 8 + b) * 12288 + col0 + col] = s + Fb_ada[(size_t)l * 12288 + col0 + col]; }
	ds_read2st64_b32 v[0:1], v33 offset1:4
	ds_read2st64_b32 v[2:3], v33 offset0:8 offset1:12
	ds_read2st64_b32 v[4:5], v33 offset0:16 offset1:20
	ds_read2st64_b32 v[6:7], v33 offset0:24 offset1:28
	ds_read2st64_b32 v[8:9], v33 offset0:32 offset1:36
	s_waitcnt lgkmcnt(4)
	v_add_f32_e32 v0, 0, v0
	v_add_f32_e32 v0, v0, v1
	s_waitcnt lgkmcnt(3)
	v_add_f32_e32 v0, v0, v2
	v_add_f32_e32 v0, v0, v3
	s_mul_i32 s9, s16, 0xc000
	s_waitcnt lgkmcnt(2)
	v_add_f32_e32 v0, v0, v4
	s_mul_hi_i32 s8, s16, 0xc000
	s_add_u32 s9, s10, s9
	v_add_f32_e32 v0, v0, v5
	s_addc_u32 s17, s3, s8
	s_waitcnt lgkmcnt(1)
	v_add_f32_e32 v0, v0, v6
	s_add_u32 s8, s9, s6
	v_add_f32_e32 v0, v0, v7
	s_addc_u32 s9, s17, s7
	s_waitcnt lgkmcnt(0)
	v_add_f32_e32 v0, v0, v8
	v_lshl_add_u64 v[4:5], s[8:9], 0, v[38:39]
	v_add_f32_e32 v6, v0, v9
	ds_read2st64_b32 v[0:1], v33 offset0:40 offset1:44
	ds_read2st64_b32 v[2:3], v33 offset0:48 offset1:52
	flat_load_dword v7, v[4:5]
	ds_read2st64_b32 v[4:5], v33 offset0:56 offset1:60
	s_waitcnt lgkmcnt(0)
	v_add_f32_e32 v0, v6, v0
	v_add_f32_e32 v0, v0, v1
	v_add_f32_e32 v2, v0, v2
	ds_read2st64_b32 v[0:1], v33 offset0:64 offset1:68
	v_add_f32_e32 v2, v2, v3
	v_add_f32_e32 v4, v2, v4
	ds_read2st64_b32 v[2:3], v33 offset0:72 offset1:76
	v_add_f32_e32 v4, v4, v5
	s_waitcnt lgkmcnt(0)
	v_add_f32_e32 v0, v4, v0
	ds_read2st64_b32 v[4:5], v33 offset0:80 offset1:84
	v_add_f32_e32 v0, v0, v1
	v_add_f32_e32 v2, v0, v2
	ds_read2st64_b32 v[0:1], v33 offset0:88 offset1:92
	v_add_f32_e32 v2, v2, v3
	s_waitcnt lgkmcnt(0)
	v_add_f32_e32 v4, v2, v4
	ds_read2st64_b32 v[2:3], v33 offset0:96 offset1:100
	v_add_f32_e32 v4, v4, v5
	v_add_f32_e32 v0, v4, v0
	ds_read2st64_b32 v[4:5], v33 offset0:104 offset1:108
	v_add_f32_e32 v0, v0, v1
	s_waitcnt lgkmcnt(0)
	v_add_f32_e32 v2, v0, v2
	ds_read2st64_b32 v[0:1], v33 offset0:112 offset1:116
	v_add_f32_e32 v2, v2, v3
	v_add_f32_e32 v4, v2, v4
	ds_read2st64_b32 v[2:3], v33 offset0:120 offset1:124
	v_add_f32_e32 v4, v4, v5
	s_waitcnt lgkmcnt(0)
	v_add_f32_e32 v0, v4, v0
	ds_read2st64_b32 v[4:5], v33 offset0:128 offset1:132
	v_add_f32_e32 v0, v0, v1
	v_add_f32_e32 v2, v0, v2
	ds_read2st64_b32 v[0:1], v33 offset0:136 offset1:140
	v_add_f32_e32 v2, v2, v3
	s_waitcnt lgkmcnt(0)
	v_add_f32_e32 v4, v2, v4
	ds_read2st64_b32 v[2:3], v33 offset0:144 offset1:148
	v_add_f32_e32 v4, v4, v5
	v_add_f32_e32 v0, v4, v0
	ds_read2st64_b32 v[4:5], v33 offset0:152 offset1:156
	v_add_f32_e32 v0, v0, v1
	s_waitcnt lgkmcnt(0)
	v_add_f32_e32 v2, v0, v2
	ds_read2st64_b32 v[0:1], v33 offset0:160 offset1:164
	v_add_f32_e32 v2, v2, v3
	v_add_f32_e32 v4, v2, v4
	ds_read2st64_b32 v[2:3], v33 offset0:168 offset1:172
	v_add_f32_e32 v4, v4, v5
	s_waitcnt lgkmcnt(0)
	v_add_f32_e32 v0, v4, v0
	ds_read2st64_b32 v[4:5], v33 offset0:176 offset1:180
	v_add_f32_e32 v0, v0, v1
	v_add_f32_e32 v2, v0, v2
	ds_read2st64_b32 v[0:1], v33 offset0:184 offset1:188
	v_add_f32_e32 v2, v2, v3
	s_waitcnt lgkmcnt(0)
	v_add_f32_e32 v4, v2, v4
	ds_read2st64_b32 v[2:3], v33 offset0:192 offset1:196
	v_add_f32_e32 v4, v4, v5
	v_add_f32_e32 v0, v4, v0
	ds_read2st64_b32 v[4:5], v33 offset0:200 offset1:204
	v_add_f32_e32 v0, v0, v1
	s_waitcnt lgkmcnt(0)
	v_add_f32_e32 v2, v0, v2
	ds_read2st64_b32 v[0:1], v33 offset0:208 offset1:212
	v_add_f32_e32 v2, v2, v3
	v_add_f32_e32 v4, v2, v4
	ds_read2st64_b32 v[2:3], v33 offset0:216 offset1:220
	v_add_f32_e32 v4, v4, v5
	s_waitcnt lgkmcnt(0)
	v_add_f32_e32 v0, v4, v0
	ds_read2st64_b32 v[4:5], v33 offset0:224 offset1:228
	v_add_f32_e32 v0, v0, v1
	v_add_f32_e32 v0, v0, v2
	v_add_f32_e32 v2, v0, v3
	ds_read2st64_b32 v[0:1], v33 offset0:232 offset1:236
	s_waitcnt lgkmcnt(0)
	v_add_f32_e32 v4, v2, v4
	ds_read2st64_b32 v[2:3], v33 offset0:240 offset1:244
	v_add_f32_e32 v6, v4, v5
	ds_read2st64_b32 v[4:5], v33 offset0:248 offset1:252
	v_add_f32_e32 v0, v6, v0
	v_add_f32_e32 v0, v0, v1
	s_waitcnt lgkmcnt(0)
	v_add_f32_e32 v0, v0, v2
	v_add_f32_e32 v0, v0, v3
	v_add_f32_e32 v0, v0, v4
	v_add_f32_e32 v0, v0, v5
	s_waitcnt vmcnt(0)
	v_add_f32_e32 v2, v0, v7
	v_lshl_add_u32 v3, s16, 3, v36
	v_mov_b64_e32 v[0:1], s[4:5]
	v_mad_i64_i32 v[0:1], s[8:9], v3, s11, v[0:1]
	v_lshl_add_u64 v[0:1], v[0:1], 0, s[6:7]
	v_lshl_add_u64 v[0:1], v[0:1], 0, v[38:39]
	global_store_dword v[0:1], v2, off
	s_branch .LBB0_19
